# k_bfinal CSR blocks: non-temporal loads for the read-once bucket array ebkt
# speedup vs baseline: 1.0160x; 1.0005x over previous
.LBB1_6:
	s_load_dwordx2 s[18:19], s[0:1], 0x10
	s_andn2_b64 vcc, exec, s[6:7]
	s_cbranch_vccnz .LBB1_40
	v_mov_b32_e32 v5, 0
	v_mov_b32_e32 v4, -1
	v_mov_b32_e32 v18, -1
	v_mov_b32_e32 v19, 0
	s_and_saveexec_b64 s[6:7], s[4:5]
	s_cbranch_execz .LBB1_9
	v_ashrrev_i32_e32 v3, 31, v2
	v_lshl_add_u64 v[6:7], v[2:3], 3, s[16:17]
	global_load_dwordx2 v[18:19], v[6:7], off nt
.LBB1_9:
	s_or_b64 exec, exec, s[6:7]
	v_add_u32_e32 v6, 0x400, v2
	v_cmp_gt_i32_e32 vcc, s25, v6
	s_and_saveexec_b64 s[6:7], vcc
	s_cbranch_execz .LBB1_11
	v_ashrrev_i32_e32 v7, 31, v6
	v_lshl_add_u64 v[4:5], v[6:7], 3, s[16:17]
	global_load_dwordx2 v[4:5], v[4:5], off nt
.LBB1_11:
	s_or_b64 exec, exec, s[6:7]
	v_add_u32_e32 v6, 0x800, v2
	v_cmp_gt_i32_e32 vcc, s25, v6
	v_mov_b32_e32 v11, 0
	v_mov_b32_e32 v10, -1
	v_mov_b32_e32 v16, -1
	v_mov_b32_e32 v17, 0
	s_and_saveexec_b64 s[6:7], vcc
	s_cbranch_execz .LBB1_13
	v_ashrrev_i32_e32 v7, 31, v6
	v_lshl_add_u64 v[6:7], v[6:7], 3, s[16:17]
	global_load_dwordx2 v[16:17], v[6:7], off nt
.LBB1_13:
	s_or_b64 exec, exec, s[6:7]
	v_add_u32_e32 v6, 0xc00, v2
	v_cmp_gt_i32_e32 vcc, s25, v6
	s_and_saveexec_b64 s[6:7], vcc
	s_cbranch_execz .LBB1_15
	v_ashrrev_i32_e32 v7, 31, v6
	v_lshl_add_u64 v[6:7], v[6:7], 3, s[16:17]
	global_load_dwordx2 v[10:11], v[6:7], off nt
.LBB1_15:
	s_or_b64 exec, exec, s[6:7]
	v_add_u32_e32 v6, 0x1000, v2
	v_cmp_gt_i32_e32 vcc, s25, v6
	v_mov_b32_e32 v9, 0
	v_mov_b32_e32 v8, -1
	v_mov_b32_e32 v14, -1
	v_mov_b32_e32 v15, 0
	s_and_saveexec_b64 s[6:7], vcc
	s_cbranch_execz .LBB1_17
	v_ashrrev_i32_e32 v7, 31, v6
	v_lshl_add_u64 v[6:7], v[6:7], 3, s[16:17]
	global_load_dwordx2 v[14:15], v[6:7], off nt
.LBB1_17:
	s_or_b64 exec, exec, s[6:7]
	v_add_u32_e32 v6, 0x1400, v2
	v_cmp_gt_i32_e32 vcc, s25, v6
	s_and_saveexec_b64 s[6:7], vcc
	s_cbranch_execz .LBB1_19
	v_ashrrev_i32_e32 v7, 31, v6
	v_lshl_add_u64 v[6:7], v[6:7], 3, s[16:17]
	global_load_dwordx2 v[8:9], v[6:7], off nt
.LBB1_19:
	s_or_b64 exec, exec, s[6:7]
	v_add_u32_e32 v20, 0x1800, v2
	v_cmp_gt_i32_e32 vcc, s25, v20
	v_mov_b32_e32 v7, 0
	v_mov_b32_e32 v6, -1
	v_mov_b32_e32 v12, -1
	v_mov_b32_e32 v13, 0
	s_and_saveexec_b64 s[6:7], vcc
	s_cbranch_execz .LBB1_21
	v_ashrrev_i32_e32 v21, 31, v20
	v_lshl_add_u64 v[12:13], v[20:21], 3, s[16:17]
	global_load_dwordx2 v[12:13], v[12:13], off nt
.LBB1_21:
	s_or_b64 exec, exec, s[6:7]
	v_add_u32_e32 v20, 0x1c00, v2
	v_cmp_gt_i32_e32 vcc, s25, v20
	s_and_saveexec_b64 s[6:7], vcc
	s_cbranch_execz .LBB1_23
	v_ashrrev_i32_e32 v21, 31, v20
	v_lshl_add_u64 v[6:7], v[20:21], 3, s[16:17]
	global_load_dwordx2 v[6:7], v[6:7], off nt
